# attention item prologue: query-norm butterfly via DPP/permlane only (v73, on top of v72)
# baseline (speedup 1.0000x reference)
.LBB0_500:
	s_andn2_b64 vcc, exec, s[8:9]
	s_cbranch_vccnz .LBB0_411
	s_cmpk_gt_i32 s54, 0x3ff
	s_mov_b64 s[6:7], 0
	s_cbranch_scc1 .LBB0_410
	s_ashr_i32 s0, s54, 31
	s_lshr_b32 s1, s0, 28
	s_add_i32 s1, s54, s1
	s_ashr_i32 s6, s1, 4
	s_and_b32 s1, s1, 0x1fffff0
	s_sub_i32 s8, s54, s1
	s_lshr_b32 s1, s6, 29
	s_add_i32 s1, s6, s1
	s_and_b32 s1, s1, -8
	s_sub_i32 s10, s6, s1
	s_lshr_b32 s0, s0, 25
	s_add_i32 s54, s54, s0
	s_add_i32 s0, s10, 1
	v_cvt_f32_i32_e32 v2, s0
	s_mov_b32 s0, 0x42fc0000
	s_ashr_i32 s6, s54, 7
	v_mov_b32_e32 v82, v0
	v_cmp_lt_f32_e32 vcc, s0, v2
	s_and_b64 s[0:1], vcc, exec
	s_cselect_b32 s0, 0xffffffc0, 0
	v_cndmask_b32_e32 v4, 0, v214, vcc
	v_sub_f32_e32 v2, v4, v2
	v_exp_f32_e32 v2, v2
	s_ashr_i32 s7, s6, 31
	s_lshl_b32 s35, s8, 7
	s_mov_b32 s37, s55
	v_ldexp_f32 v4, v2, s0
	s_lshl_b64 s[0:1], s[6:7], 11
	s_ashr_i32 s7, s35, 31
	s_add_u32 s86, s0, s35
	s_addc_u32 s87, s1, s7
	s_mul_i32 s0, s87, 0x2c00
	s_mul_hi_u32 s1, s86, 0x2c00
	s_add_i32 s1, s1, s0
	s_mul_i32 s0, s86, 0x2c00
	s_add_u32 s7, s24, s0
	s_addc_u32 s8, s25, s1
	s_lshl_b32 s0, s10, 7
	s_ashr_i32 s1, s0, 31
	s_lshl_b64 s[88:89], s[0:1], 1
	s_add_u32 s0, s7, s88
	s_addc_u32 s1, s8, s89
	s_add_u32 s8, s0, 0x1400
	s_addc_u32 s9, s1, 0
	v_readfirstlane_b32 s55, v82
	s_ashr_i32 s82, s55, 7
	s_ashr_i32 s54, s55, 6
	v_and_b32_e32 v216, 31, v82
	s_lshl_b32 s0, s82, 5
	s_and_b32 s1, s54, 1
	v_or_b32_e32 v2, s0, v216
	v_mov_b64_e32 v[6:7], s[8:9]
	s_movk_i32 s7, 0x2c00
	v_bfe_u32 v221, v82, 5, 1
	v_mad_i64_i32 v[6:7], s[8:9], v2, s7, v[6:7]
	s_lshl_b32 s40, s1, 7
	v_lshl_add_u64 v[6:7], v[6:7], 0, s[40:41]
	v_lshlrev_b32_e32 v2, 4, v221
	v_lshl_add_u64 v[6:7], v[6:7], 0, v[2:3]
	global_load_dwordx4 v[130:133], v[6:7], off
	global_load_dwordx4 v[134:137], v[6:7], off offset:32
	global_load_dwordx4 v[138:141], v[6:7], off offset:64
	global_load_dwordx4 v[142:145], v[6:7], off offset:96
	v_and_b32_e32 v223, 63, v82
	s_barrier
	s_waitcnt vmcnt(3)
	v_and_b32_e32 v5, 0xffff0000, v130
	v_lshlrev_b32_e32 v2, 16, v130
	v_mul_f32_e32 v6, v5, v5
	v_fmac_f32_e32 v6, v2, v2
	v_lshlrev_b32_e32 v2, 16, v131
	v_fmac_f32_e32 v6, v2, v2
	v_and_b32_e32 v2, 0xffff0000, v131
	v_fmac_f32_e32 v6, v2, v2
	v_lshlrev_b32_e32 v2, 16, v132
	v_fmac_f32_e32 v6, v2, v2
	v_and_b32_e32 v2, 0xffff0000, v132
	v_fmac_f32_e32 v6, v2, v2
	v_lshlrev_b32_e32 v2, 16, v133
	v_fmac_f32_e32 v6, v2, v2
	v_and_b32_e32 v2, 0xffff0000, v133
	v_fmac_f32_e32 v6, v2, v2
	s_waitcnt vmcnt(2)
	v_lshlrev_b32_e32 v2, 16, v134
	v_fmac_f32_e32 v6, v2, v2
	v_and_b32_e32 v2, 0xffff0000, v134
	v_fmac_f32_e32 v6, v2, v2
	v_lshlrev_b32_e32 v2, 16, v135
	v_fmac_f32_e32 v6, v2, v2
	v_and_b32_e32 v2, 0xffff0000, v135
	v_fmac_f32_e32 v6, v2, v2
	v_lshlrev_b32_e32 v2, 16, v136
	v_fmac_f32_e32 v6, v2, v2
	v_and_b32_e32 v2, 0xffff0000, v136
	v_fmac_f32_e32 v6, v2, v2
	v_lshlrev_b32_e32 v2, 16, v137
	v_fmac_f32_e32 v6, v2, v2
	v_and_b32_e32 v2, 0xffff0000, v137
	v_fmac_f32_e32 v6, v2, v2
	s_waitcnt vmcnt(1)
	v_lshlrev_b32_e32 v2, 16, v138
	v_fmac_f32_e32 v6, v2, v2
	v_and_b32_e32 v2, 0xffff0000, v138
	v_fmac_f32_e32 v6, v2, v2
	v_lshlrev_b32_e32 v2, 16, v139
	v_fmac_f32_e32 v6, v2, v2
	v_and_b32_e32 v2, 0xffff0000, v139
	v_fmac_f32_e32 v6, v2, v2
	v_lshlrev_b32_e32 v2, 16, v140
	v_fmac_f32_e32 v6, v2, v2
	v_and_b32_e32 v2, 0xffff0000, v140
	v_fmac_f32_e32 v6, v2, v2
	v_lshlrev_b32_e32 v2, 16, v141
	v_fmac_f32_e32 v6, v2, v2
	v_and_b32_e32 v2, 0xffff0000, v141
	v_fmac_f32_e32 v6, v2, v2
	s_waitcnt vmcnt(0)
	v_lshlrev_b32_e32 v2, 16, v142
	v_fmac_f32_e32 v6, v2, v2
	v_and_b32_e32 v2, 0xffff0000, v142
	v_fmac_f32_e32 v6, v2, v2
	v_lshlrev_b32_e32 v2, 16, v143
	v_fmac_f32_e32 v6, v2, v2
	v_and_b32_e32 v2, 0xffff0000, v143
	v_fmac_f32_e32 v6, v2, v2
	v_lshlrev_b32_e32 v2, 16, v144
	v_fmac_f32_e32 v6, v2, v2
	v_and_b32_e32 v2, 0xffff0000, v144
	v_fmac_f32_e32 v6, v2, v2
	v_lshlrev_b32_e32 v2, 16, v145
	v_fmac_f32_e32 v6, v2, v2
	v_and_b32_e32 v2, 0xffff0000, v145
	v_and_b32_e32 v5, 64, v212
	v_fmac_f32_e32 v6, v2, v2
	v_xor_b32_e32 v2, 32, v212
	v_add_u32_e32 v5, 64, v5
	v_cmp_lt_i32_e32 vcc, v2, v5
	s_nop 1
	v_cndmask_b32_e32 v2, v212, v2, vcc
	v_lshlrev_b32_e32 v2, 2, v2
	v_mov_b32_e32 v7, v6
	s_nop 1
	v_permlane32_swap_b32_e32 v7, v6
	s_waitcnt lgkmcnt(0)
	v_add_f32_e32 v6, v6, v7
	v_xor_b32_e32 v7, 16, v212
	v_cmp_lt_i32_e32 vcc, v7, v5
	s_nop 1
	v_cndmask_b32_e32 v7, v212, v7, vcc
	v_lshlrev_b32_e32 v217, 2, v7
	v_mov_b32_e32 v7, v6
	s_nop 1
	v_permlane16_swap_b32_e32 v7, v6
	s_waitcnt lgkmcnt(0)
	v_max_f32_e32 v7, v7, v7
	v_max_f32_e32 v6, v6, v7
	v_xor_b32_e32 v7, 8, v212
	v_cmp_lt_i32_e32 vcc, v7, v5
	s_nop 1
	v_cndmask_b32_e32 v7, v212, v7, vcc
	v_lshlrev_b32_e32 v218, 2, v7
	s_nop 1
	v_mov_b32_dpp v7, v6 row_ror:8 row_mask:0xf bank_mask:0xf
	s_waitcnt lgkmcnt(0)
	v_max_f32_e32 v7, v7, v7
	v_max_f32_e32 v6, v6, v7
	v_xor_b32_e32 v7, 4, v212
	v_cmp_lt_i32_e32 vcc, v7, v5
	s_nop 1
	v_cndmask_b32_e32 v7, v212, v7, vcc
	v_lshlrev_b32_e32 v219, 2, v7
	s_nop 1
	v_mov_b32_dpp v7, v6 row_shr:4 row_mask:0xf bank_mask:0xa
	v_mov_b32_dpp v7, v6 row_shl:4 row_mask:0xf bank_mask:0x5
	s_waitcnt lgkmcnt(0)
	v_max_f32_e32 v7, v7, v7
	v_max_f32_e32 v6, v6, v7
	v_xor_b32_e32 v7, 2, v212
	v_cmp_lt_i32_e32 vcc, v7, v5
	s_nop 1
	v_cndmask_b32_e32 v7, v212, v7, vcc
	v_lshlrev_b32_e32 v220, 2, v7
	s_nop 1
	v_mov_b32_dpp v7, v6 quad_perm:[2,3,0,1] row_mask:0xf bank_mask:0xf
	s_waitcnt lgkmcnt(0)
	v_max_f32_e32 v7, v7, v7
	v_max_f32_e32 v6, v6, v7
	v_xor_b32_e32 v7, 1, v212
	v_cmp_lt_i32_e32 vcc, v7, v5
	s_nop 1
	v_cndmask_b32_e32 v5, v212, v7, vcc
	v_lshlrev_b32_e32 v222, 2, v5
	s_nop 1
	v_mov_b32_dpp v5, v6 quad_perm:[1,0,3,2] row_mask:0xf bank_mask:0xf
	v_cmp_eq_u32_e32 vcc, 0, v223
	s_and_saveexec_b64 s[8:9], vcc
	s_cbranch_execz .LBB0_504
	s_lshl_b32 s7, s54, 2
	s_add_i32 s7, s7, 0
	s_waitcnt lgkmcnt(0)
	v_max_f32_e32 v5, v5, v5
	v_max_f32_e32 v6, v6, v6
	s_add_i32 s7, s7, 0x18c00
	v_max_f32_e32 v5, v6, v5
	v_mov_b32_e32 v6, s7
	ds_write_b32 v6, v5
